# P10 prologue: gathered-row table rt filled with all units' LIST loads in flight at once (lane-parallel table lookups) instead of 17 serial LDS+global round trips
# speedup vs baseline: 1.0089x; 1.0089x over previous
; template <class Epi, class Sched, bool F8 = false, bool MID = false, bool GATHER = false>
; __device__ __forceinline__ void gemm_phase(LAS unsigned char* lds, const Gemm g, const Sched& S, const Epi& E) {
;     ...
;     if constexpr (GATHER) { Unit uu;
;         for (int i = 0; i < 20 && S.next(i, uu); ++i) if (tid < 256) { const int l_ = uu.row0 - g.tab[uu.e] + tid; rt[i * 256 + tid] = l_ < g.tab[32 + uu.e] ? g.list[uu.e * T + l_] : T; }
;         asm volatile("s_waitcnt vmcnt(0) lgkmcnt(0)" ::: "memory"); __builtin_amdgcn_s_barrier(); asm volatile("" ::: "memory");
.LBB0_2358:
	s_load_dwordx2 s[50:51], s[0:1], 0x80
	s_load_dwordx2 s[52:53], s[0:1], 0x90
	s_mov_b32 s13, 0x20000
	v_mbcnt_lo_u32_b32 v1, -1, 0
	v_mbcnt_hi_u32_b32 v1, -1, v1
	v_mul_lo_u32 v2, v1, s82
	v_add_u32_e32 v2, s2, v2
	v_cmp_gt_i32_e32 vcc, s39, v2
	v_lshrrev_b32_e32 v3, 4, v2
	v_min_u32_e32 v4, 0x13f, v3
	v_lshlrev_b32_e32 v4, 2, v4
	v_add_u32_e32 v4, 0x25a04, v4
	ds_read_b32 v5, v4
	s_mov_b64 s[54:55], vcc
	s_waitcnt lgkmcnt(0)
	v_lshlrev_b32_e32 v6, 2, v5
	v_add_u32_e32 v6, 0x25800, v6
	ds_read2_b32 v[6:7], v6 offset1:32
	v_lshlrev_b32_e32 v3, 8, v3
	v_cmp_gt_u32_e32 vcc, 0x100, v0
	v_lshl_add_u32 v1, v0, 2, s13
	s_mov_b64 s[56:57], vcc
	s_waitcnt lgkmcnt(0)
	v_sub_u32_e32 v3, v3, v6
	s_bitcmp1_b32 s54, 0
	s_cbranch_scc0 .Lrt_issued
	v_readlane_b32 s4, v5, 0
	v_readlane_b32 s5, v3, 0
	v_readlane_b32 s22, v7, 0
	v_mov_b32_e32 v200, 0x4000
	s_nop 1
	v_add_u32_e32 v8, s5, v0
	v_cmp_gt_i32_e32 vcc, s22, v8
	s_lshl_b32 s4, s4, 14
	s_nop 0
	s_and_b64 vcc, vcc, s[56:57]
	v_add_lshl_u32 v8, v8, s4, 2
	s_and_saveexec_b64 s[26:27], vcc
	global_load_dword v200, v8, s[48:49]
	s_mov_b64 exec, s[26:27]
	s_bitcmp1_b32 s54, 1
	s_cbranch_scc0 .Lrt_issued
	v_readlane_b32 s4, v5, 1
	v_readlane_b32 s5, v3, 1
	v_readlane_b32 s22, v7, 1
	v_mov_b32_e32 v201, 0x4000
	s_nop 1
	v_add_u32_e32 v8, s5, v0
	v_cmp_gt_i32_e32 vcc, s22, v8
	s_lshl_b32 s4, s4, 14
	s_nop 0
	s_and_b64 vcc, vcc, s[56:57]
	v_add_lshl_u32 v8, v8, s4, 2
	s_and_saveexec_b64 s[26:27], vcc
	global_load_dword v201, v8, s[48:49]
	s_mov_b64 exec, s[26:27]
	s_bitcmp1_b32 s54, 2
	s_cbranch_scc0 .Lrt_issued
	v_readlane_b32 s4, v5, 2
	v_readlane_b32 s5, v3, 2
	v_readlane_b32 s22, v7, 2
	v_mov_b32_e32 v202, 0x4000
	s_nop 1
	v_add_u32_e32 v8, s5, v0
	v_cmp_gt_i32_e32 vcc, s22, v8
	s_lshl_b32 s4, s4, 14
	s_nop 0
	s_and_b64 vcc, vcc, s[56:57]
	v_add_lshl_u32 v8, v8, s4, 2
	s_and_saveexec_b64 s[26:27], vcc
	global_load_dword v202, v8, s[48:49]
	s_mov_b64 exec, s[26:27]
	s_bitcmp1_b32 s54, 3
	s_cbranch_scc0 .Lrt_issued
	v_readlane_b32 s4, v5, 3
	v_readlane_b32 s5, v3, 3
	v_readlane_b32 s22, v7, 3
	v_mov_b32_e32 v203, 0x4000
	s_nop 1
	v_add_u32_e32 v8, s5, v0
	v_cmp_gt_i32_e32 vcc, s22, v8
	s_lshl_b32 s4, s4, 14
	s_nop 0
	s_and_b64 vcc, vcc, s[56:57]
	v_add_lshl_u32 v8, v8, s4, 2
	s_and_saveexec_b64 s[26:27], vcc
	global_load_dword v203, v8, s[48:49]
	s_mov_b64 exec, s[26:27]
	s_bitcmp1_b32 s54, 4
	s_cbranch_scc0 .Lrt_issued
	v_readlane_b32 s4, v5, 4
	v_readlane_b32 s5, v3, 4
	v_readlane_b32 s22, v7, 4
	v_mov_b32_e32 v204, 0x4000
	s_nop 1
	v_add_u32_e32 v8, s5, v0
	v_cmp_gt_i32_e32 vcc, s22, v8
	s_lshl_b32 s4, s4, 14
	s_nop 0
	s_and_b64 vcc, vcc, s[56:57]
	v_add_lshl_u32 v8, v8, s4, 2
	s_and_saveexec_b64 s[26:27], vcc
	global_load_dword v204, v8, s[48:49]
	s_mov_b64 exec, s[26:27]
	s_bitcmp1_b32 s54, 5
	s_cbranch_scc0 .Lrt_issued
	v_readlane_b32 s4, v5, 5
	v_readlane_b32 s5, v3, 5
	v_readlane_b32 s22, v7, 5
	v_mov_b32_e32 v205, 0x4000
	s_nop 1
	v_add_u32_e32 v8, s5, v0
	v_cmp_gt_i32_e32 vcc, s22, v8
	s_lshl_b32 s4, s4, 14
	s_nop 0
	s_and_b64 vcc, vcc, s[56:57]
	v_add_lshl_u32 v8, v8, s4, 2
	s_and_saveexec_b64 s[26:27], vcc
	global_load_dword v205, v8, s[48:49]
	s_mov_b64 exec, s[26:27]
	s_bitcmp1_b32 s54, 6
	s_cbranch_scc0 .Lrt_issued
	v_readlane_b32 s4, v5, 6
	v_readlane_b32 s5, v3, 6
	v_readlane_b32 s22, v7, 6
	v_mov_b32_e32 v206, 0x4000
	s_nop 1
	v_add_u32_e32 v8, s5, v0
	v_cmp_gt_i32_e32 vcc, s22, v8
	s_lshl_b32 s4, s4, 14
	s_nop 0
	s_and_b64 vcc, vcc, s[56:57]
	v_add_lshl_u32 v8, v8, s4, 2
	s_and_saveexec_b64 s[26:27], vcc
	global_load_dword v206, v8, s[48:49]
	s_mov_b64 exec, s[26:27]
	s_bitcmp1_b32 s54, 7
	s_cbranch_scc0 .Lrt_issued
	v_readlane_b32 s4, v5, 7
	v_readlane_b32 s5, v3, 7
	v_readlane_b32 s22, v7, 7
	v_mov_b32_e32 v207, 0x4000
	s_nop 1
	v_add_u32_e32 v8, s5, v0
	v_cmp_gt_i32_e32 vcc, s22, v8
	s_lshl_b32 s4, s4, 14
	s_nop 0
	s_and_b64 vcc, vcc, s[56:57]
	v_add_lshl_u32 v8, v8, s4, 2
	s_and_saveexec_b64 s[26:27], vcc
	global_load_dword v207, v8, s[48:49]
	s_mov_b64 exec, s[26:27]
	s_bitcmp1_b32 s54, 8
	s_cbranch_scc0 .Lrt_issued
	v_readlane_b32 s4, v5, 8
	v_readlane_b32 s5, v3, 8
	v_readlane_b32 s22, v7, 8
	v_mov_b32_e32 v208, 0x4000
	s_nop 1
	v_add_u32_e32 v8, s5, v0
	v_cmp_gt_i32_e32 vcc, s22, v8
	s_lshl_b32 s4, s4, 14
	s_nop 0
	s_and_b64 vcc, vcc, s[56:57]
	v_add_lshl_u32 v8, v8, s4, 2
	s_and_saveexec_b64 s[26:27], vcc
	global_load_dword v208, v8, s[48:49]
	s_mov_b64 exec, s[26:27]
	s_bitcmp1_b32 s54, 9
	s_cbranch_scc0 .Lrt_issued
	v_readlane_b32 s4, v5, 9
	v_readlane_b32 s5, v3, 9
	v_readlane_b32 s22, v7, 9
	v_mov_b32_e32 v209, 0x4000
	s_nop 1
	v_add_u32_e32 v8, s5, v0
	v_cmp_gt_i32_e32 vcc, s22, v8
	s_lshl_b32 s4, s4, 14
	s_nop 0
	s_and_b64 vcc, vcc, s[56:57]
	v_add_lshl_u32 v8, v8, s4, 2
	s_and_saveexec_b64 s[26:27], vcc
	global_load_dword v209, v8, s[48:49]
	s_mov_b64 exec, s[26:27]
	s_bitcmp1_b32 s54, 10
	s_cbranch_scc0 .Lrt_issued
	v_readlane_b32 s4, v5, 10
	v_readlane_b32 s5, v3, 10
	v_readlane_b32 s22, v7, 10
	v_mov_b32_e32 v210, 0x4000
	s_nop 1
	v_add_u32_e32 v8, s5, v0
	v_cmp_gt_i32_e32 vcc, s22, v8
	s_lshl_b32 s4, s4, 14
	s_nop 0
	s_and_b64 vcc, vcc, s[56:57]
	v_add_lshl_u32 v8, v8, s4, 2
	s_and_saveexec_b64 s[26:27], vcc
	global_load_dword v210, v8, s[48:49]
	s_mov_b64 exec, s[26:27]
	s_bitcmp1_b32 s54, 11
	s_cbranch_scc0 .Lrt_issued
; template <class Epi, class Sched, bool F8 = false, bool MID = false, bool GATHER = false>
; __device__ __forceinline__ void gemm_phase(LAS unsigned char* lds, const Gemm g, const Sched& S, const Epi& E) {
;     ...
;         for (int i = 0; i < 20 && S.next(i, uu); ++i) if (tid < 256) { const int l_ = uu.row0 - g.tab[uu.e] + tid; rt[i * 256 + tid] = l_ < g.tab[32 + uu.e] ? g.list[uu.e * T + l_] : T; }
;         asm volatile("s_waitcnt vmcnt(0) lgkmcnt(0)" ::: "memory"); __builtin_amdgcn_s_barrier(); asm volatile("" ::: "memory");
	v_readlane_b32 s4, v5, 11
	v_readlane_b32 s5, v3, 11
	v_readlane_b32 s22, v7, 11
	v_mov_b32_e32 v211, 0x4000
	s_nop 1
	v_add_u32_e32 v8, s5, v0
	v_cmp_gt_i32_e32 vcc, s22, v8
	s_lshl_b32 s4, s4, 14
	s_nop 0
	s_and_b64 vcc, vcc, s[56:57]
	v_add_lshl_u32 v8, v8, s4, 2
	s_and_saveexec_b64 s[26:27], vcc
	global_load_dword v211, v8, s[48:49]
	s_mov_b64 exec, s[26:27]
	s_bitcmp1_b32 s54, 12
	s_cbranch_scc0 .Lrt_issued
	v_readlane_b32 s4, v5, 12
	v_readlane_b32 s5, v3, 12
	v_readlane_b32 s22, v7, 12
	v_mov_b32_e32 v212, 0x4000
	s_nop 1
	v_add_u32_e32 v8, s5, v0
	v_cmp_gt_i32_e32 vcc, s22, v8
	s_lshl_b32 s4, s4, 14
	s_nop 0
	s_and_b64 vcc, vcc, s[56:57]
	v_add_lshl_u32 v8, v8, s4, 2
	s_and_saveexec_b64 s[26:27], vcc
	global_load_dword v212, v8, s[48:49]
	s_mov_b64 exec, s[26:27]
	s_bitcmp1_b32 s54, 13
	s_cbranch_scc0 .Lrt_issued
	v_readlane_b32 s4, v5, 13
	v_readlane_b32 s5, v3, 13
	v_readlane_b32 s22, v7, 13
	v_mov_b32_e32 v213, 0x4000
	s_nop 1
	v_add_u32_e32 v8, s5, v0
	v_cmp_gt_i32_e32 vcc, s22, v8
	s_lshl_b32 s4, s4, 14
	s_nop 0
	s_and_b64 vcc, vcc, s[56:57]
	v_add_lshl_u32 v8, v8, s4, 2
	s_and_saveexec_b64 s[26:27], vcc
	global_load_dword v213, v8, s[48:49]
	s_mov_b64 exec, s[26:27]
	s_bitcmp1_b32 s54, 14
	s_cbranch_scc0 .Lrt_issued
	v_readlane_b32 s4, v5, 14
	v_readlane_b32 s5, v3, 14
	v_readlane_b32 s22, v7, 14
	v_mov_b32_e32 v214, 0x4000
	s_nop 1
	v_add_u32_e32 v8, s5, v0
	v_cmp_gt_i32_e32 vcc, s22, v8
	s_lshl_b32 s4, s4, 14
	s_nop 0
	s_and_b64 vcc, vcc, s[56:57]
	v_add_lshl_u32 v8, v8, s4, 2
	s_and_saveexec_b64 s[26:27], vcc
	global_load_dword v214, v8, s[48:49]
	s_mov_b64 exec, s[26:27]
	s_bitcmp1_b32 s54, 15
	s_cbranch_scc0 .Lrt_issued
	v_readlane_b32 s4, v5, 15
	v_readlane_b32 s5, v3, 15
	v_readlane_b32 s22, v7, 15
	v_mov_b32_e32 v215, 0x4000
	s_nop 1
	v_add_u32_e32 v8, s5, v0
	v_cmp_gt_i32_e32 vcc, s22, v8
	s_lshl_b32 s4, s4, 14
	s_nop 0
	s_and_b64 vcc, vcc, s[56:57]
	v_add_lshl_u32 v8, v8, s4, 2
	s_and_saveexec_b64 s[26:27], vcc
	global_load_dword v215, v8, s[48:49]
	s_mov_b64 exec, s[26:27]
	s_bitcmp1_b32 s54, 16
	s_cbranch_scc0 .Lrt_issued
	v_readlane_b32 s4, v5, 16
	v_readlane_b32 s5, v3, 16
	v_readlane_b32 s22, v7, 16
	v_mov_b32_e32 v216, 0x4000
	s_nop 1
	v_add_u32_e32 v8, s5, v0
	v_cmp_gt_i32_e32 vcc, s22, v8
	s_lshl_b32 s4, s4, 14
	s_nop 0
	s_and_b64 vcc, vcc, s[56:57]
	v_add_lshl_u32 v8, v8, s4, 2
	s_and_saveexec_b64 s[26:27], vcc
	global_load_dword v216, v8, s[48:49]
	s_mov_b64 exec, s[26:27]
	s_bitcmp1_b32 s54, 17
	s_cbranch_scc0 .Lrt_issued
	v_readlane_b32 s4, v5, 17
	v_readlane_b32 s5, v3, 17
	v_readlane_b32 s22, v7, 17
	v_mov_b32_e32 v217, 0x4000
	s_nop 1
	v_add_u32_e32 v8, s5, v0
	v_cmp_gt_i32_e32 vcc, s22, v8
	s_lshl_b32 s4, s4, 14
	s_nop 0
	s_and_b64 vcc, vcc, s[56:57]
	v_add_lshl_u32 v8, v8, s4, 2
	s_and_saveexec_b64 s[26:27], vcc
	global_load_dword v217, v8, s[48:49]
	s_mov_b64 exec, s[26:27]
	s_bitcmp1_b32 s54, 18
	s_cbranch_scc0 .Lrt_issued
	v_readlane_b32 s4, v5, 18
	v_readlane_b32 s5, v3, 18
	v_readlane_b32 s22, v7, 18
	v_mov_b32_e32 v218, 0x4000
	s_nop 1
	v_add_u32_e32 v8, s5, v0
	v_cmp_gt_i32_e32 vcc, s22, v8
	s_lshl_b32 s4, s4, 14
	s_nop 0
	s_and_b64 vcc, vcc, s[56:57]
	v_add_lshl_u32 v8, v8, s4, 2
	s_and_saveexec_b64 s[26:27], vcc
	global_load_dword v218, v8, s[48:49]
	s_mov_b64 exec, s[26:27]
	s_bitcmp1_b32 s54, 19
	s_cbranch_scc0 .Lrt_issued
	v_readlane_b32 s4, v5, 19
	v_readlane_b32 s5, v3, 19
	v_readlane_b32 s22, v7, 19
	v_mov_b32_e32 v219, 0x4000
	s_nop 1
	v_add_u32_e32 v8, s5, v0
	v_cmp_gt_i32_e32 vcc, s22, v8
	s_lshl_b32 s4, s4, 14
	s_nop 0
	s_and_b64 vcc, vcc, s[56:57]
	v_add_lshl_u32 v8, v8, s4, 2
	s_and_saveexec_b64 s[26:27], vcc
	global_load_dword v219, v8, s[48:49]
	s_mov_b64 exec, s[26:27]
.Lrt_issued:
	s_and_saveexec_b64 s[26:27], s[56:57]
	s_waitcnt vmcnt(0)
	s_bitcmp1_b32 s54, 0
	s_cbranch_scc0 .Lrt_done
	ds_write_b32 v1, v200
	s_bitcmp1_b32 s54, 1
	s_cbranch_scc0 .Lrt_done
	ds_write_b32 v1, v201 offset:1024
	s_bitcmp1_b32 s54, 2
	s_cbranch_scc0 .Lrt_done
	ds_write_b32 v1, v202 offset:2048
	s_bitcmp1_b32 s54, 3
	s_cbranch_scc0 .Lrt_done
	ds_write_b32 v1, v203 offset:3072
	s_bitcmp1_b32 s54, 4
	s_cbranch_scc0 .Lrt_done
	ds_write_b32 v1, v204 offset:4096
	s_bitcmp1_b32 s54, 5
	s_cbranch_scc0 .Lrt_done
	ds_write_b32 v1, v205 offset:5120
	s_bitcmp1_b32 s54, 6
	s_cbranch_scc0 .Lrt_done
	ds_write_b32 v1, v206 offset:6144
	s_bitcmp1_b32 s54, 7
	s_cbranch_scc0 .Lrt_done
	ds_write_b32 v1, v207 offset:7168
	s_bitcmp1_b32 s54, 8
	s_cbranch_scc0 .Lrt_done
	ds_write_b32 v1, v208 offset:8192
	s_bitcmp1_b32 s54, 9
	s_cbranch_scc0 .Lrt_done
	ds_write_b32 v1, v209 offset:9216
	s_bitcmp1_b32 s54, 10
	s_cbranch_scc0 .Lrt_done
	ds_write_b32 v1, v210 offset:10240
	s_bitcmp1_b32 s54, 11
	s_cbranch_scc0 .Lrt_done
	ds_write_b32 v1, v211 offset:11264
	s_bitcmp1_b32 s54, 12
	s_cbranch_scc0 .Lrt_done
	ds_write_b32 v1, v212 offset:12288
	s_bitcmp1_b32 s54, 13
	s_cbranch_scc0 .Lrt_done
	ds_write_b32 v1, v213 offset:13312
	s_bitcmp1_b32 s54, 14
	s_cbranch_scc0 .Lrt_done
	ds_write_b32 v1, v214 offset:14336
	s_bitcmp1_b32 s54, 15
	s_cbranch_scc0 .Lrt_done
	ds_write_b32 v1, v215 offset:15360
	s_bitcmp1_b32 s54, 16
	s_cbranch_scc0 .Lrt_done
	ds_write_b32 v1, v216 offset:16384
	s_bitcmp1_b32 s54, 17
	s_cbranch_scc0 .Lrt_done
	ds_write_b32 v1, v217 offset:17408
	s_bitcmp1_b32 s54, 18
	s_cbranch_scc0 .Lrt_done
	ds_write_b32 v1, v218 offset:18432
	s_bitcmp1_b32 s54, 19
	s_cbranch_scc0 .Lrt_done
	ds_write_b32 v1, v219 offset:19456
.Lrt_done:
	s_mov_b64 exec, s[26:27]
